# E32: E24 + back-edge rotation of the NSA far loops applied only to the low-priority wave group (tid<256); the priority-1 waves keep the original post-barrier head
# speedup vs baseline: 1.0027x; 1.0019x over previous
.LBB0_697:
	v_sub_f32_e32 v0, v5, v134
	v_fmamk_f32 v5, v98, 0x3fb8aa3b, v0
	v_exp_f32_e32 v98, v5
	v_fmamk_f32 v5, v99, 0x3fb8aa3b, v0
	v_exp_f32_e32 v99, v5
	v_fmamk_f32 v5, v100, 0x3fb8aa3b, v0
	v_exp_f32_e32 v100, v5
	v_fmamk_f32 v5, v101, 0x3fb8aa3b, v0
	v_exp_f32_e32 v101, v5
	v_fmamk_f32 v94, v94, 0x3fb8aa3b, v0
	v_add_f32_e32 v5, 0, v98
	v_exp_f32_e32 v94, v94
	v_fmamk_f32 v95, v95, 0x3fb8aa3b, v0
	v_add_f32_e32 v5, v99, v5
	v_exp_f32_e32 v95, v95
	v_fmamk_f32 v96, v96, 0x3fb8aa3b, v0
	v_add_f32_e32 v5, v100, v5
	v_exp_f32_e32 v96, v96
	v_fmamk_f32 v97, v97, 0x3fb8aa3b, v0
	v_add_f32_e32 v5, v101, v5
	v_exp_f32_e32 v97, v97
	v_fmamk_f32 v90, v90, 0x3fb8aa3b, v0
	v_add_f32_e32 v5, v94, v5
	v_exp_f32_e32 v90, v90
	v_fmamk_f32 v91, v91, 0x3fb8aa3b, v0
	v_add_f32_e32 v5, v95, v5
	v_exp_f32_e32 v91, v91
	v_fmamk_f32 v92, v92, 0x3fb8aa3b, v0
	v_add_f32_e32 v5, v96, v5
	v_exp_f32_e32 v92, v92
	v_fmamk_f32 v93, v93, 0x3fb8aa3b, v0
	v_add_f32_e32 v5, v97, v5
	v_exp_f32_e32 v93, v93
	v_fmamk_f32 v86, v86, 0x3fb8aa3b, v0
	v_add_f32_e32 v5, v90, v5
	v_exp_f32_e32 v198, v86
	v_fmamk_f32 v86, v87, 0x3fb8aa3b, v0
	v_add_f32_e32 v5, v91, v5
	v_exp_f32_e32 v199, v86
	v_fmamk_f32 v86, v88, 0x3fb8aa3b, v0
	v_add_f32_e32 v5, v92, v5
	v_exp_f32_e32 v200, v86
	v_fmac_f32_e32 v0, 0x3fb8aa3b, v89
	v_add_f32_e32 v5, v93, v5
	v_exp_f32_e32 v0, v0
	v_add_f32_e32 v5, v198, v5
	v_add_f32_e32 v5, v199, v5
	v_add_f32_e32 v5, v200, v5
	v_add_f32_e32 v5, v0, v5
	v_fmac_f32_e32 v5, v136, v4
	v_sub_f32_e32 v4, v137, v125
	v_fmamk_f32 v82, v82, 0x3fb8aa3b, v4
	v_exp_f32_e32 v82, v82
	v_fmamk_f32 v83, v83, 0x3fb8aa3b, v4
	v_exp_f32_e32 v83, v83
	v_fmamk_f32 v84, v84, 0x3fb8aa3b, v4
	v_exp_f32_e32 v84, v84
	v_fmamk_f32 v85, v85, 0x3fb8aa3b, v4
	v_exp_f32_e32 v85, v85
	v_fmamk_f32 v78, v78, 0x3fb8aa3b, v4
	v_add_f32_e32 v86, 0, v82
	v_exp_f32_e32 v87, v78
	v_fmamk_f32 v78, v79, 0x3fb8aa3b, v4
	v_add_f32_e32 v86, v83, v86
	v_exp_f32_e32 v88, v78
	v_fmamk_f32 v78, v80, 0x3fb8aa3b, v4
	v_add_f32_e32 v86, v84, v86
	v_exp_f32_e32 v89, v78
	v_fmamk_f32 v78, v81, 0x3fb8aa3b, v4
	v_add_f32_e32 v86, v85, v86
	v_exp_f32_e32 v81, v78
	v_fmamk_f32 v74, v74, 0x3fb8aa3b, v4
	v_add_f32_e32 v78, v87, v86
	v_exp_f32_e32 v136, v74
	v_fmamk_f32 v74, v75, 0x3fb8aa3b, v4
	v_add_f32_e32 v78, v88, v78
	v_exp_f32_e32 v137, v74
	v_fmamk_f32 v74, v76, 0x3fb8aa3b, v4
	v_add_f32_e32 v78, v89, v78
	v_exp_f32_e32 v201, v74
	v_fmamk_f32 v74, v77, 0x3fb8aa3b, v4
	v_add_f32_e32 v78, v81, v78
	v_exp_f32_e32 v202, v74
	v_fmamk_f32 v70, v70, 0x3fb8aa3b, v4
	v_add_f32_e32 v74, v136, v78
	v_exp_f32_e32 v203, v70
	v_fmamk_f32 v70, v71, 0x3fb8aa3b, v4
	v_add_f32_e32 v74, v137, v74
	v_exp_f32_e32 v204, v70
	v_fmamk_f32 v70, v72, 0x3fb8aa3b, v4
	v_add_f32_e32 v74, v201, v74
	v_exp_f32_e32 v205, v70
	v_fmac_f32_e32 v4, 0x3fb8aa3b, v73
	v_add_f32_e32 v74, v202, v74
	v_exp_f32_e32 v4, v4
	v_add_f32_e32 v70, v203, v74
	s_cmp_eq_u32 s83, 0
	v_add_f32_e32 v70, v204, v70
	v_add_f32_e32 v70, v205, v70
	s_cselect_b32 s0, 0x8000, s79
	v_add_f32_e32 v133, v4, v70
	s_add_i32 s0, s0, 0
	v_fmac_f32_e32 v133, v135, v2
	v_add_u32_e32 v2, s0, v142
	ds_read_b128 v[70:73], v2
	ds_read_b128 v[74:77], v2 offset:2048
	v_cvt_pk_bf16_f32 v78, v82, v83
	v_cvt_pk_bf16_f32 v79, v84, v85
	ds_read_b128 v[82:85], v2 offset:4096
	v_cvt_pk_bf16_f32 v80, v87, v88
	v_cvt_pk_bf16_f32 v81, v89, v81
	v_cvt_pk_bf16_f32 v86, v98, v99
	v_cvt_pk_bf16_f32 v87, v100, v101
	v_cvt_pk_bf16_f32 v88, v94, v95
	v_cvt_pk_bf16_f32 v89, v96, v97
	s_waitcnt lgkmcnt(2)
	v_mfma_f32_16x16x32_bf16 v[66:69], v[70:73], v[78:81], v[66:69]
	v_mfma_f32_16x16x32_bf16 v[34:37], v[70:73], v[86:89], v[34:37]
	ds_read_b128 v[70:73], v2 offset:6144
	s_waitcnt lgkmcnt(2)
	v_mfma_f32_16x16x32_bf16 v[62:65], v[74:77], v[78:81], v[62:65]
	v_mfma_f32_16x16x32_bf16 v[30:33], v[74:77], v[86:89], v[30:33]
	ds_read_b128 v[74:77], v2 offset:8192
	s_waitcnt lgkmcnt(2)
	v_mfma_f32_16x16x32_bf16 v[58:61], v[82:85], v[78:81], v[58:61]
	v_mfma_f32_16x16x32_bf16 v[26:29], v[82:85], v[86:89], v[26:29]
	ds_read_b128 v[82:85], v2 offset:10240
	s_waitcnt lgkmcnt(2)
	v_mfma_f32_16x16x32_bf16 v[54:57], v[70:73], v[78:81], v[54:57]
	v_mfma_f32_16x16x32_bf16 v[22:25], v[70:73], v[86:89], v[22:25]
	ds_read_b128 v[70:73], v2 offset:12288
	s_waitcnt lgkmcnt(2)
	v_mfma_f32_16x16x32_bf16 v[50:53], v[74:77], v[78:81], v[50:53]
	v_mfma_f32_16x16x32_bf16 v[18:21], v[74:77], v[86:89], v[18:21]
	ds_read_b128 v[74:77], v2 offset:14336
	v_add_u32_e32 v2, s0, v146
	s_waitcnt lgkmcnt(2)
	v_mfma_f32_16x16x32_bf16 v[46:49], v[82:85], v[78:81], v[46:49]
	v_mfma_f32_16x16x32_bf16 v[14:17], v[82:85], v[86:89], v[14:17]
	ds_read_b128 v[82:85], v2
	s_waitcnt lgkmcnt(2)
	v_mfma_f32_16x16x32_bf16 v[42:45], v[70:73], v[78:81], v[42:45]
	v_mfma_f32_16x16x32_bf16 v[10:13], v[70:73], v[86:89], v[10:13]
	ds_read_b128 v[70:73], v2 offset:2048
	s_waitcnt lgkmcnt(2)
	v_mfma_f32_16x16x32_bf16 v[38:41], v[74:77], v[78:81], v[38:41]
	v_cvt_pk_bf16_f32 v78, v90, v91
	v_cvt_pk_bf16_f32 v79, v92, v93
	v_cvt_pk_bf16_f32 v80, v198, v199
	v_mfma_f32_16x16x32_bf16 v[6:9], v[74:77], v[86:89], v[6:9]
	ds_read_b128 v[86:89], v2 offset:4096
	v_cvt_pk_bf16_f32 v74, v136, v137
	v_cvt_pk_bf16_f32 v75, v201, v202
	v_cvt_pk_bf16_f32 v76, v203, v204
	v_cvt_pk_bf16_f32 v77, v205, v4
	v_cvt_pk_bf16_f32 v81, v200, v0
	s_nop 0
	s_waitcnt lgkmcnt(2)
	v_mfma_f32_16x16x32_bf16 v[66:69], v[82:85], v[74:77], v[66:69]
	v_mfma_f32_16x16x32_bf16 v[34:37], v[82:85], v[78:81], v[34:37]
	ds_read_b128 v[82:85], v2 offset:6144
	s_waitcnt lgkmcnt(2)
	v_mfma_f32_16x16x32_bf16 v[62:65], v[70:73], v[74:77], v[62:65]
	v_mfma_f32_16x16x32_bf16 v[30:33], v[70:73], v[78:81], v[30:33]
	ds_read_b128 v[70:73], v2 offset:8192
	s_waitcnt lgkmcnt(2)
	v_mfma_f32_16x16x32_bf16 v[58:61], v[86:89], v[74:77], v[58:61]
	v_mfma_f32_16x16x32_bf16 v[26:29], v[86:89], v[78:81], v[26:29]
	ds_read_b128 v[86:89], v2 offset:10240
	s_waitcnt lgkmcnt(2)
	v_mfma_f32_16x16x32_bf16 v[54:57], v[82:85], v[74:77], v[54:57]
	v_mfma_f32_16x16x32_bf16 v[22:25], v[82:85], v[78:81], v[22:25]
	ds_read_b128 v[82:85], v2 offset:12288
	s_waitcnt lgkmcnt(2)
	v_mfma_f32_16x16x32_bf16 v[50:53], v[70:73], v[74:77], v[50:53]
	v_mfma_f32_16x16x32_bf16 v[18:21], v[70:73], v[78:81], v[18:21]
	ds_read_b128 v[70:73], v2 offset:14336
	s_waitcnt lgkmcnt(2)
	v_mfma_f32_16x16x32_bf16 v[46:49], v[86:89], v[74:77], v[46:49]
	v_mfma_f32_16x16x32_bf16 v[14:17], v[86:89], v[78:81], v[14:17]
	s_waitcnt lgkmcnt(1)
	v_mfma_f32_16x16x32_bf16 v[42:45], v[82:85], v[74:77], v[42:45]
	v_mfma_f32_16x16x32_bf16 v[10:13], v[82:85], v[78:81], v[10:13]
	s_waitcnt lgkmcnt(0)
	v_mfma_f32_16x16x32_bf16 v[38:41], v[70:73], v[74:77], v[38:41]
	s_waitcnt vmcnt(0)
	s_add_i32 s33, s33, 1
	s_add_i32 s0, s8, s33
	v_mfma_f32_16x16x32_bf16 v[6:9], v[70:73], v[78:81], v[6:9]
	s_cmp_eq_u32 s0, 1
	s_cbranch_scc1 .Lx687_exit
	v_readfirstlane_b32 s98, v226
	s_cmpk_lt_u32 s98, 0x100
	s_cbranch_scc0 .Lx687_orig
	v_mov_b32_e32 v136, v5
	v_mov_b32_e32 v135, v133
	v_mov_b32_e32 v133, v125
	v_mov_b32_e32 v4, v134
	s_add_i32 s0, s33, -1
	s_and_b32 s83, s0, 1
	s_add_i32 s3, s3, 1
	s_lshl_b32 s0, s83, 14
	s_add_i32 s0, s0, 0
	v_add_u32_e32 v0, s0, v140
	s_add_i32 s1, s37, s33
	s_add_i32 s1, s1, -1
	s_mov_b32 s32, 0
	s_add_i32 s98, s33, -1
	s_cmp_ge_u32 s98, s86
	s_cbranch_scc1 .Lx687_pd
	s_cmp_ge_i32 s33, s42
	s_mov_b64 s[98:99], -1
	s_cbranch_scc0 .Lx687_a
	s_add_i32 s98, s8, s33
	s_cmp_ge_i32 s98, s43
	s_cselect_b32 s99, s82, 0
	s_add_i32 s22, s98, s99
	s_mov_b64 s[98:99], 0

.LBB0_805:
	v_sub_f32_e32 v0, v125, v134
	v_fmamk_f32 v5, v98, 0x3fb8aa3b, v0
	v_exp_f32_e32 v98, v5
	v_fmamk_f32 v5, v99, 0x3fb8aa3b, v0
	v_exp_f32_e32 v99, v5
	v_fmamk_f32 v5, v100, 0x3fb8aa3b, v0
	v_exp_f32_e32 v100, v5
	v_fmamk_f32 v5, v101, 0x3fb8aa3b, v0
	v_exp_f32_e32 v101, v5
	v_fmamk_f32 v94, v94, 0x3fb8aa3b, v0
	v_add_f32_e32 v5, 0, v98
	v_exp_f32_e32 v94, v94
	v_fmamk_f32 v95, v95, 0x3fb8aa3b, v0
	v_add_f32_e32 v5, v99, v5
	v_exp_f32_e32 v95, v95
	v_fmamk_f32 v96, v96, 0x3fb8aa3b, v0
	v_add_f32_e32 v5, v100, v5
	v_exp_f32_e32 v96, v96
	v_fmamk_f32 v97, v97, 0x3fb8aa3b, v0
	v_add_f32_e32 v5, v101, v5
	v_exp_f32_e32 v97, v97
	v_fmamk_f32 v90, v90, 0x3fb8aa3b, v0
	v_add_f32_e32 v5, v94, v5
	v_exp_f32_e32 v90, v90
	v_fmamk_f32 v91, v91, 0x3fb8aa3b, v0
	v_add_f32_e32 v5, v95, v5
	v_exp_f32_e32 v91, v91
	v_fmamk_f32 v92, v92, 0x3fb8aa3b, v0
	v_add_f32_e32 v5, v96, v5
	v_exp_f32_e32 v92, v92
	v_fmamk_f32 v93, v93, 0x3fb8aa3b, v0
	v_add_f32_e32 v5, v97, v5
	v_exp_f32_e32 v93, v93
	v_fmamk_f32 v86, v86, 0x3fb8aa3b, v0
	v_add_f32_e32 v5, v90, v5
	v_exp_f32_e32 v137, v86
	v_fmamk_f32 v86, v87, 0x3fb8aa3b, v0
	v_add_f32_e32 v5, v91, v5
	v_exp_f32_e32 v198, v86
	v_fmamk_f32 v86, v88, 0x3fb8aa3b, v0
	v_add_f32_e32 v5, v92, v5
	v_exp_f32_e32 v199, v86
	v_fmac_f32_e32 v0, 0x3fb8aa3b, v89
	v_add_f32_e32 v5, v93, v5
	v_exp_f32_e32 v0, v0
	v_add_f32_e32 v5, v137, v5
	v_add_f32_e32 v5, v198, v5
	v_add_f32_e32 v5, v199, v5
	v_add_f32_e32 v5, v0, v5
	v_fmac_f32_e32 v5, v136, v4
	v_sub_f32_e32 v4, v125, v133
	v_fmamk_f32 v82, v82, 0x3fb8aa3b, v4
	v_exp_f32_e32 v82, v82
	v_fmamk_f32 v83, v83, 0x3fb8aa3b, v4
	v_exp_f32_e32 v83, v83
	v_fmamk_f32 v84, v84, 0x3fb8aa3b, v4
	v_exp_f32_e32 v84, v84
	v_fmamk_f32 v85, v85, 0x3fb8aa3b, v4
	v_exp_f32_e32 v85, v85
	v_fmamk_f32 v78, v78, 0x3fb8aa3b, v4
	v_add_f32_e32 v86, 0, v82
	v_exp_f32_e32 v87, v78
	v_fmamk_f32 v78, v79, 0x3fb8aa3b, v4
	v_add_f32_e32 v86, v83, v86
	v_exp_f32_e32 v88, v78
	v_fmamk_f32 v78, v80, 0x3fb8aa3b, v4
	v_add_f32_e32 v86, v84, v86
	v_exp_f32_e32 v89, v78
	v_fmamk_f32 v78, v81, 0x3fb8aa3b, v4
	v_add_f32_e32 v86, v85, v86
	v_exp_f32_e32 v81, v78
	v_fmamk_f32 v74, v74, 0x3fb8aa3b, v4
	v_add_f32_e32 v78, v87, v86
	v_exp_f32_e32 v136, v74
	v_fmamk_f32 v74, v75, 0x3fb8aa3b, v4
	v_add_f32_e32 v78, v88, v78
	v_exp_f32_e32 v200, v74
	v_fmamk_f32 v74, v76, 0x3fb8aa3b, v4
	v_add_f32_e32 v78, v89, v78
	v_exp_f32_e32 v201, v74
	v_fmamk_f32 v74, v77, 0x3fb8aa3b, v4
	v_add_f32_e32 v78, v81, v78
	v_exp_f32_e32 v202, v74
	v_fmamk_f32 v70, v70, 0x3fb8aa3b, v4
	v_add_f32_e32 v74, v136, v78
	v_exp_f32_e32 v203, v70
	v_fmamk_f32 v70, v71, 0x3fb8aa3b, v4
	v_add_f32_e32 v74, v200, v74
	v_exp_f32_e32 v204, v70
	v_fmamk_f32 v70, v72, 0x3fb8aa3b, v4
	v_add_f32_e32 v74, v201, v74
	v_exp_f32_e32 v205, v70
	v_fmac_f32_e32 v4, 0x3fb8aa3b, v73
	v_add_f32_e32 v74, v202, v74
	v_exp_f32_e32 v4, v4
	v_add_f32_e32 v70, v203, v74
	s_cmp_eq_u32 s81, 0
	v_add_f32_e32 v70, v204, v70
	v_add_f32_e32 v70, v205, v70
	s_cselect_b32 s0, 0x8000, s79
	v_add_f32_e32 v125, v4, v70
	s_add_i32 s0, s0, 0
	v_fmac_f32_e32 v125, v135, v2
	v_add_u32_e32 v2, s0, v142
	ds_read_b128 v[70:73], v2
	ds_read_b128 v[74:77], v2 offset:2048
	v_cvt_pk_bf16_f32 v78, v82, v83
	v_cvt_pk_bf16_f32 v79, v84, v85
	ds_read_b128 v[82:85], v2 offset:4096
	v_cvt_pk_bf16_f32 v80, v87, v88
	v_cvt_pk_bf16_f32 v81, v89, v81
	v_cvt_pk_bf16_f32 v86, v98, v99
	v_cvt_pk_bf16_f32 v87, v100, v101
	v_cvt_pk_bf16_f32 v88, v94, v95
	v_cvt_pk_bf16_f32 v89, v96, v97
	s_waitcnt lgkmcnt(2)
	v_mfma_f32_16x16x32_bf16 v[66:69], v[70:73], v[78:81], v[66:69]
	v_mfma_f32_16x16x32_bf16 v[34:37], v[70:73], v[86:89], v[34:37]
	ds_read_b128 v[70:73], v2 offset:6144
	s_waitcnt lgkmcnt(2)
	v_mfma_f32_16x16x32_bf16 v[62:65], v[74:77], v[78:81], v[62:65]
	v_mfma_f32_16x16x32_bf16 v[30:33], v[74:77], v[86:89], v[30:33]
	ds_read_b128 v[74:77], v2 offset:8192
	s_waitcnt lgkmcnt(2)
	v_mfma_f32_16x16x32_bf16 v[58:61], v[82:85], v[78:81], v[58:61]
	v_mfma_f32_16x16x32_bf16 v[26:29], v[82:85], v[86:89], v[26:29]
	ds_read_b128 v[82:85], v2 offset:10240
	s_waitcnt lgkmcnt(2)
	v_mfma_f32_16x16x32_bf16 v[54:57], v[70:73], v[78:81], v[54:57]
	v_mfma_f32_16x16x32_bf16 v[22:25], v[70:73], v[86:89], v[22:25]
	ds_read_b128 v[70:73], v2 offset:12288
	s_waitcnt lgkmcnt(2)
	v_mfma_f32_16x16x32_bf16 v[50:53], v[74:77], v[78:81], v[50:53]
	v_mfma_f32_16x16x32_bf16 v[18:21], v[74:77], v[86:89], v[18:21]
	ds_read_b128 v[74:77], v2 offset:14336
	v_add_u32_e32 v2, s0, v146
	s_waitcnt lgkmcnt(2)
	v_mfma_f32_16x16x32_bf16 v[46:49], v[82:85], v[78:81], v[46:49]
	v_mfma_f32_16x16x32_bf16 v[14:17], v[82:85], v[86:89], v[14:17]
	ds_read_b128 v[82:85], v2
	s_waitcnt lgkmcnt(2)
	v_mfma_f32_16x16x32_bf16 v[42:45], v[70:73], v[78:81], v[42:45]
	v_mfma_f32_16x16x32_bf16 v[10:13], v[70:73], v[86:89], v[10:13]
	ds_read_b128 v[70:73], v2 offset:2048
	s_waitcnt lgkmcnt(2)
	v_mfma_f32_16x16x32_bf16 v[38:41], v[74:77], v[78:81], v[38:41]
	v_cvt_pk_bf16_f32 v78, v90, v91
	v_cvt_pk_bf16_f32 v79, v92, v93
	v_cvt_pk_bf16_f32 v80, v137, v198
	v_mfma_f32_16x16x32_bf16 v[6:9], v[74:77], v[86:89], v[6:9]
	ds_read_b128 v[86:89], v2 offset:4096
	v_cvt_pk_bf16_f32 v74, v136, v200
	v_cvt_pk_bf16_f32 v75, v201, v202
	v_cvt_pk_bf16_f32 v76, v203, v204
	v_cvt_pk_bf16_f32 v77, v205, v4
	v_cvt_pk_bf16_f32 v81, v199, v0
	s_nop 0
	s_waitcnt lgkmcnt(2)
	v_mfma_f32_16x16x32_bf16 v[66:69], v[82:85], v[74:77], v[66:69]
	v_mfma_f32_16x16x32_bf16 v[34:37], v[82:85], v[78:81], v[34:37]
	ds_read_b128 v[82:85], v2 offset:6144
	s_waitcnt lgkmcnt(2)
	v_mfma_f32_16x16x32_bf16 v[62:65], v[70:73], v[74:77], v[62:65]
	v_mfma_f32_16x16x32_bf16 v[30:33], v[70:73], v[78:81], v[30:33]
	ds_read_b128 v[70:73], v2 offset:8192
	s_waitcnt lgkmcnt(2)
	v_mfma_f32_16x16x32_bf16 v[58:61], v[86:89], v[74:77], v[58:61]
	v_mfma_f32_16x16x32_bf16 v[26:29], v[86:89], v[78:81], v[26:29]
	ds_read_b128 v[86:89], v2 offset:10240
	s_waitcnt lgkmcnt(2)
	v_mfma_f32_16x16x32_bf16 v[54:57], v[82:85], v[74:77], v[54:57]
	v_mfma_f32_16x16x32_bf16 v[22:25], v[82:85], v[78:81], v[22:25]
	ds_read_b128 v[82:85], v2 offset:12288
	s_waitcnt lgkmcnt(2)
	v_mfma_f32_16x16x32_bf16 v[50:53], v[70:73], v[74:77], v[50:53]
	v_mfma_f32_16x16x32_bf16 v[18:21], v[70:73], v[78:81], v[18:21]
	ds_read_b128 v[70:73], v2 offset:14336
	s_waitcnt lgkmcnt(2)
	v_mfma_f32_16x16x32_bf16 v[46:49], v[86:89], v[74:77], v[46:49]
	v_mfma_f32_16x16x32_bf16 v[14:17], v[86:89], v[78:81], v[14:17]
	s_waitcnt lgkmcnt(1)
	v_mfma_f32_16x16x32_bf16 v[42:45], v[82:85], v[74:77], v[42:45]
	v_mfma_f32_16x16x32_bf16 v[10:13], v[82:85], v[78:81], v[10:13]
	s_waitcnt lgkmcnt(0)
	v_mfma_f32_16x16x32_bf16 v[38:41], v[70:73], v[74:77], v[38:41]
	s_waitcnt vmcnt(0)
	s_add_i32 s0, s3, s47
	s_cmp_lg_u32 s0, 0
	v_mfma_f32_16x16x32_bf16 v[6:9], v[70:73], v[78:81], v[6:9]
	s_cbranch_scc0 .Lx791_exit
	v_readfirstlane_b32 s98, v226
	s_cmpk_lt_u32 s98, 0x100
	s_cbranch_scc0 .Lx791_orig
	s_mov_b32 s32, 0
	v_mov_b32_e32 v136, v5
	v_mov_b32_e32 v135, v125
	v_mov_b32_e32 v137, v133
	v_mov_b32_e32 v4, v134
	s_mov_b32 s22, s47
	s_and_b32 s81, s22, 1
	s_add_i32 s47, s22, 1
	s_cmp_ge_i32 s22, s93
	s_cbranch_scc1 .Lx791_pd
